# speedup vs baseline: 1.0373x; 1.0043x over previous
.LBB0_9:
	ds_read_b128 v[10:13], v8
	ds_read_b128 v[14:17], v8 offset:16
	ds_read_b128 v[30:33], v8 offset:32
	ds_read_b128 v[34:37], v8 offset:48
	ds_read_b128 v[40:43], v9
	ds_read_b128 v[44:47], v9 offset:16
	ds_read_b128 v[48:51], v9 offset:32
	ds_read_b128 v[52:55], v9 offset:48
	ds_read_b128 v[56:59], v9 offset:272
	ds_read_b128 v[60:63], v9 offset:288
	ds_read_b128 v[64:67], v9 offset:544
	ds_read_b128 v[68:71], v9 offset:560
	ds_read_b128 v[72:75], v9 offset:816
	ds_read_b128 v[76:79], v9 offset:832
	ds_read_b128 v[80:83], v9 offset:304
	ds_read_b128 v[84:87], v9 offset:320
	ds_read_b128 v[88:91], v9 offset:576
	ds_read_b128 v[92:95], v9 offset:592
	ds_read_b128 v[96:99], v9 offset:848
	ds_read_b128 v[100:103], v9 offset:864
	s_waitcnt lgkmcnt(0)
	v_fmac_f32_e32 v7, v10, v40
	v_fmac_f32_e32 v6, v10, v56
	v_fmac_f32_e32 v1, v10, v64
	v_fmac_f32_e32 v0, v10, v72
	v_fmac_f32_e32 v7, v11, v41
	v_fmac_f32_e32 v6, v11, v57
	v_fmac_f32_e32 v1, v11, v65
	v_fmac_f32_e32 v0, v11, v73
	v_fmac_f32_e32 v7, v12, v42
	v_fmac_f32_e32 v6, v12, v58
	v_fmac_f32_e32 v1, v12, v66
	v_fmac_f32_e32 v0, v12, v74
	v_fmac_f32_e32 v7, v13, v43
	v_fmac_f32_e32 v6, v13, v59
	v_fmac_f32_e32 v1, v13, v67
	v_fmac_f32_e32 v0, v13, v75
	v_fmac_f32_e32 v7, v14, v44
	v_fmac_f32_e32 v6, v14, v60
	v_fmac_f32_e32 v1, v14, v68
	v_fmac_f32_e32 v0, v14, v76
	v_fmac_f32_e32 v7, v15, v45
	v_fmac_f32_e32 v6, v15, v61
	v_fmac_f32_e32 v1, v15, v69
	v_fmac_f32_e32 v0, v15, v77
	v_fmac_f32_e32 v7, v16, v46
	v_fmac_f32_e32 v6, v16, v62
	v_fmac_f32_e32 v1, v16, v70
	v_fmac_f32_e32 v0, v16, v78
	v_fmac_f32_e32 v7, v17, v47
	v_fmac_f32_e32 v6, v17, v63
	v_fmac_f32_e32 v1, v17, v71
	v_fmac_f32_e32 v0, v17, v79
	v_fmac_f32_e32 v7, v30, v48
	v_fmac_f32_e32 v6, v30, v80
	v_fmac_f32_e32 v1, v30, v88
	v_fmac_f32_e32 v0, v30, v96
	v_fmac_f32_e32 v7, v31, v49
	v_fmac_f32_e32 v6, v31, v81
	v_fmac_f32_e32 v1, v31, v89
	v_fmac_f32_e32 v0, v31, v97
	v_fmac_f32_e32 v7, v32, v50
	v_fmac_f32_e32 v6, v32, v82
	v_fmac_f32_e32 v1, v32, v90
	v_fmac_f32_e32 v0, v32, v98
	v_fmac_f32_e32 v7, v33, v51
	v_fmac_f32_e32 v6, v33, v83
	v_fmac_f32_e32 v1, v33, v91
	v_fmac_f32_e32 v0, v33, v99
	v_fmac_f32_e32 v7, v34, v52
	v_fmac_f32_e32 v6, v34, v84
	v_fmac_f32_e32 v1, v34, v92
	v_fmac_f32_e32 v0, v34, v100
	v_fmac_f32_e32 v7, v35, v53
	v_fmac_f32_e32 v6, v35, v85
	v_fmac_f32_e32 v1, v35, v93
	v_fmac_f32_e32 v0, v35, v101
	v_fmac_f32_e32 v7, v36, v54
	v_fmac_f32_e32 v6, v36, v86
	v_fmac_f32_e32 v1, v36, v94
	v_fmac_f32_e32 v0, v36, v102
	v_fmac_f32_e32 v7, v37, v55
	v_fmac_f32_e32 v6, v37, v87
	v_fmac_f32_e32 v1, v37, v95
	v_fmac_f32_e32 v0, v37, v103
	s_add_i32 s79, s79, 16
	v_add_u32_e32 v9, 64, v9
	v_add_u32_e32 v8, 64, v8
	s_cmp_lt_u32 s79, 60
	s_cbranch_scc1 .LBB0_9
	v_pk_mul_f32 v[6:7], v[6:7], s[68:69] op_sel_hi:[1,0]
	v_pk_mul_f32 v[0:1], v[0:1], s[68:69] op_sel_hi:[1,0]

.LBB0_59:
	s_endpgm
	s_endpgm
	s_endpgm
	s_endpgm
	s_endpgm
	s_endpgm
	s_endpgm
	s_endpgm
	s_endpgm
	s_endpgm
	s_endpgm
	s_endpgm
	s_endpgm
	s_endpgm
	s_endpgm
	s_endpgm
	s_endpgm
	s_endpgm
	.section	.rodata,"a",@progbits
	.p2align	6, 0x0

.LBB4_13:
	ds_read_b128 v[12:15], v9
	ds_read_b128 v[16:19], v9 offset:16
	ds_read_b128 v[20:23], v9 offset:32
	ds_read_b128 v[24:27], v9 offset:48
	ds_read_b128 v[28:31], v10
	ds_read_b128 v[32:35], v10 offset:16
	ds_read_b128 v[36:39], v10 offset:32
	ds_read_b128 v[40:43], v10 offset:48
	ds_read_b128 v[62:65], v10 offset:272
	ds_read_b128 v[72:75], v10 offset:288
	ds_read_b128 v[44:47], v10 offset:544
	ds_read_b128 v[48:51], v10 offset:560
	ds_read_b128 v[68:71], v10 offset:816
	ds_read_b128 v[78:81], v10 offset:832
	ds_read_b128 v[82:85], v10 offset:304
	ds_read_b128 v[92:95], v10 offset:320
	ds_read_b128 v[52:55], v10 offset:576
	ds_read_b128 v[56:59], v10 offset:592
	ds_read_b128 v[88:91], v10 offset:848
	ds_read_b128 v[98:101], v10 offset:864
	s_waitcnt lgkmcnt(0)
	v_fmac_f32_e32 v5, v12, v28
	v_fmac_f32_e32 v4, v12, v62
	v_fmac_f32_e32 v3, v12, v44
	v_fmac_f32_e32 v2, v12, v68
	v_fmac_f32_e32 v5, v13, v29
	v_fmac_f32_e32 v4, v13, v63
	v_fmac_f32_e32 v3, v13, v45
	v_fmac_f32_e32 v2, v13, v69
	v_fmac_f32_e32 v5, v14, v30
	v_fmac_f32_e32 v4, v14, v64
	v_fmac_f32_e32 v3, v14, v46
	v_fmac_f32_e32 v2, v14, v70
	v_fmac_f32_e32 v5, v15, v31
	v_fmac_f32_e32 v4, v15, v65
	v_fmac_f32_e32 v3, v15, v47
	v_fmac_f32_e32 v2, v15, v71
	v_fmac_f32_e32 v5, v16, v32
	v_fmac_f32_e32 v4, v16, v72
	v_fmac_f32_e32 v3, v16, v48
	v_fmac_f32_e32 v2, v16, v78
	v_fmac_f32_e32 v5, v17, v33
	v_fmac_f32_e32 v4, v17, v73
	v_fmac_f32_e32 v3, v17, v49
	v_fmac_f32_e32 v2, v17, v79
	v_fmac_f32_e32 v5, v18, v34
	v_fmac_f32_e32 v4, v18, v74
	v_fmac_f32_e32 v3, v18, v50
	v_fmac_f32_e32 v2, v18, v80
	v_fmac_f32_e32 v5, v19, v35
	v_fmac_f32_e32 v4, v19, v75
	v_fmac_f32_e32 v3, v19, v51
	v_fmac_f32_e32 v2, v19, v81
	v_fmac_f32_e32 v5, v20, v36
	v_fmac_f32_e32 v4, v20, v82
	v_fmac_f32_e32 v3, v20, v52
	v_fmac_f32_e32 v2, v20, v88
	v_fmac_f32_e32 v5, v21, v37
	v_fmac_f32_e32 v4, v21, v83
	v_fmac_f32_e32 v3, v21, v53
	v_fmac_f32_e32 v2, v21, v89
	v_fmac_f32_e32 v5, v22, v38
	v_fmac_f32_e32 v4, v22, v84
	v_fmac_f32_e32 v3, v22, v54
	v_fmac_f32_e32 v2, v22, v90
	v_fmac_f32_e32 v5, v23, v39
	v_fmac_f32_e32 v4, v23, v85
	v_fmac_f32_e32 v3, v23, v55
	v_fmac_f32_e32 v2, v23, v91
	v_fmac_f32_e32 v5, v24, v40
	v_fmac_f32_e32 v4, v24, v92
	v_fmac_f32_e32 v3, v24, v56
	v_fmac_f32_e32 v2, v24, v98
	v_fmac_f32_e32 v5, v25, v41
	v_fmac_f32_e32 v4, v25, v93
	v_fmac_f32_e32 v3, v25, v57
	v_fmac_f32_e32 v2, v25, v99
	v_fmac_f32_e32 v5, v26, v42
	v_fmac_f32_e32 v4, v26, v94
	v_fmac_f32_e32 v3, v26, v58
	v_fmac_f32_e32 v2, v26, v100
	v_fmac_f32_e32 v5, v27, v43
	v_fmac_f32_e32 v4, v27, v95
	v_fmac_f32_e32 v3, v27, v59
	v_fmac_f32_e32 v2, v27, v101
	s_add_i32 s8, s8, 16
	v_add_u32_e32 v9, 64, v9
	v_add_u32_e32 v10, 64, v10
	s_cmp_lt_u32 s8, 60
	s_cbranch_scc1 .LBB4_13
	s_mov_b32 s8, 0x3e000000
	v_pk_mul_f32 v[4:5], v[4:5], s[8:9] op_sel_hi:[1,0]
	v_pk_mul_f32 v[2:3], v[2:3], s[8:9] op_sel_hi:[1,0]

.LBB4_64:
	s_mov_b32 s12, 0
	s_mov_b32 s11, 1
	s_mov_b32 s8, 0
	s_bitcmp1_b32 s9, 1
	s_cbranch_scc0 .LBB4_6
	s_branch .LBB4_7
	s_endpgm
	s_endpgm
	s_endpgm
	s_endpgm
	s_endpgm
	s_endpgm
	s_endpgm
	s_endpgm
	s_endpgm
	s_endpgm
	s_endpgm
	s_endpgm
	s_endpgm
	s_endpgm
	s_endpgm
	s_endpgm
	s_endpgm
	s_endpgm
	s_endpgm
	s_endpgm
	s_endpgm
	s_endpgm
	s_endpgm
	s_endpgm
	s_endpgm
	s_endpgm
	s_endpgm
	s_endpgm
	s_endpgm
	s_endpgm
	s_endpgm
	s_endpgm
	s_endpgm
	s_endpgm
	s_endpgm
	s_endpgm
	s_endpgm
	s_endpgm
	s_endpgm
	s_endpgm
	s_endpgm
	s_endpgm
	s_endpgm
	s_endpgm
	s_endpgm
	.section	.rodata,"a",@progbits
	.p2align	6, 0x0
